# finish phase: 16-lane butterfly reductions via DPP (quad_perm/row_half_mirror/row_mirror) instead of ds_bpermute round trips; bit-identical
# baseline (speedup 1.0000x reference)
; __device__ __forceinline__ float siluf_(float x) { return x * __builtin_amdgcn_rcpf(1.f + fexp(-x)); }
; __device__ __forceinline__ float lo16(unsigned u) { return __uint_as_float(u << 16); }
; __device__ void phase_finish(const Params& p, int l, char* smem, int vb, int nvb, int oz) {
;     ...
;     for (int row = rbeg; row < rend; ++row) {
;         bf16_t* ur = U + (size_t)row * LDU;
;         const u32x2 rf = nl[0], rb = nl[1], gf = nl[2], gb = nl[3], zg = nl[4], zr = nl[5];
; #pragma unroll
;         for (int i = 0; i < 6; ++i) nl[i] = nm[i];
;         if (row + 2 < rend) F_LOAD(nm, row + 2)
;         {
;             const float o0 = lo16(gf[0]) + lo16(gb[0]), o1 = hi16(gf[0]) + hi16(gb[0]);
;             const float o2 = lo16(gf[1]) + lo16(gb[1]), o3 = hi16(gf[1]) + hi16(gb[1]);
;             float ss = o0 * o0 + o1 * o1 + o2 * o2 + o3 * o3;
;             ss += __shfl_xor(ss, 1); ss += __shfl_xor(ss, 2); ss += __shfl_xor(ss, 4); ss += __shfl_xor(ss, 8);
;             const float rs = rsqrtf(ss * (1.f / 64.f) + EPS);
;             u32x2 y;
;             y[0] = cvt_pk(o0 * rs * ng.x * siluf_(lo16(zg[0])), o1 * rs * ng.y * siluf_(hi16(zg[0])));
;             y[1] = cvt_pk(o2 * rs * ng.z * siluf_(lo16(zg[1])), o3 * rs * ng.w * siluf_(hi16(zg[1])));
;             st_wt8(ur + C_GZ + lane * 4, y);
;         }
;         {
;             const float o0 = lo16(rf[0]) + lo16(rb[0]), o1 = hi16(rf[0]) + hi16(rb[0]);
;             const float o2 = lo16(rf[1]) + lo16(rb[1]), o3 = hi16(rf[1]) + hi16(rb[1]);
;             float s1 = o0 + o1 + o2 + o3;
;             s1 += __shfl_xor(s1, 1); s1 += __shfl_xor(s1, 2); s1 += __shfl_xor(s1, 4); s1 += __shfl_xor(s1, 8);
;             const float mu = s1 * (1.f / 64.f);
;             const float d0 = o0 - mu, d1 = o1 - mu, d2 = o2 - mu, d3 = o3 - mu;
;             float s2 = d0 * d0 + d1 * d1 + d2 * d2 + d3 * d3;
;             s2 += __shfl_xor(s2, 1); s2 += __shfl_xor(s2, 2); s2 += __shfl_xor(s2, 4); s2 += __shfl_xor(s2, 8);
;             const float rs = rsqrtf(s2 * (1.f / 64.f) + EPS);
;             u32x2 y;
;             y[0] = cvt_pk(d0 * rs * siluf_(lo16(zr[0])), d1 * rs * siluf_(hi16(zr[0])));
;             y[1] = cvt_pk(d2 * rs * siluf_(lo16(zr[1])), d3 * rs * siluf_(hi16(zr[1])));
;             st_wt8(ur + C_RZ + lane * 4, y);
;         }
.LBB0_245:
	v_lshlrev_b32_e32 v56, 16, v41
	v_and_b32_e32 v57, 0xffff0000, v41
	v_lshlrev_b32_e32 v58, 16, v39
	v_and_b32_e32 v59, 0xffff0000, v39
	v_pk_add_f32 v[56:57], v[58:59], v[56:57]
	v_lshlrev_b32_e32 v58, 16, v40
	v_and_b32_e32 v59, 0xffff0000, v40
	v_lshlrev_b32_e32 v40, 16, v38
	v_and_b32_e32 v41, 0xffff0000, v38
	v_pk_add_f32 v[38:39], v[40:41], v[58:59]
	v_lshlrev_b32_e32 v54, 16, v30
	v_and_b32_e32 v55, 0xffff0000, v30
	v_add_f32_e32 v30, v38, v39
	v_add_f32_e32 v30, v56, v30
	v_add_f32_e32 v30, v57, v30
	v_lshlrev_b32_e32 v50, 16, v33
	v_and_b32_e32 v51, 0xffff0000, v33
	v_mul_f32_e32 v40, 0xbfb8aa3b, v54
	v_mul_f32_e32 v41, 0xbfb8aa3b, v55
	v_lshlrev_b32_e32 v48, 16, v43
	v_and_b32_e32 v49, 0xffff0000, v43
	v_add_f32_dpp v30, v30, v30 quad_perm:[1,0,3,2] row_mask:0xf bank_mask:0xf
	v_lshlrev_b32_e32 v52, 16, v42
	v_and_b32_e32 v53, 0xffff0000, v42
	v_lshlrev_b32_e32 v42, 16, v32
	v_exp_f32_e32 v40, v40
	v_add_f32_dpp v30, v30, v30 quad_perm:[2,3,0,1] row_mask:0xf bank_mask:0xf
	v_exp_f32_e32 v41, v41
	v_and_b32_e32 v43, 0xffff0000, v32
	v_pk_add_f32 v[32:33], v[42:43], v[52:53]
	v_add_f32_e32 v40, 1.0, v40
	v_add_f32_dpp v52, v30, v30 row_half_mirror row_mask:0xf bank_mask:0xf
	v_add_f32_e32 v41, 1.0, v41
	v_rcp_f32_e32 v40, v40
	v_rcp_f32_e32 v41, v41
	v_lshlrev_b32_e32 v30, 16, v31
	v_add_f32_dpp v52, v52, v52 row_mirror row_mask:0xf bank_mask:0xf
	v_mul_f32_e32 v52, 0x3c800000, v52
	v_pk_mul_f32 v[40:41], v[40:41], v[54:55]
	v_mul_f32_e32 v54, 0xbfb8aa3b, v30
	v_pk_add_f32 v[38:39], v[38:39], v[52:53] op_sel_hi:[1,0] neg_lo:[0,1] neg_hi:[0,1]
	v_pk_add_f32 v[48:49], v[50:51], v[48:49]
	v_pk_mul_f32 v[42:43], v[32:33], v[32:33]
	v_exp_f32_e32 v60, v54
	v_pk_add_f32 v[52:53], v[56:57], v[52:53] op_sel_hi:[1,0] neg_lo:[0,1] neg_hi:[0,1]
	v_pk_mul_f32 v[54:55], v[38:39], v[38:39]
	v_pk_mul_f32 v[50:51], v[48:49], v[48:49]
	v_pk_mul_f32 v[56:57], v[52:53], v[52:53]
	v_mov_b32_e32 v58, v54
	v_mov_b32_e32 v59, v42
	v_mov_b32_e32 v42, v55
	v_pk_add_f32 v[42:43], v[58:59], v[42:43]
	v_mov_b32_e32 v54, v56
	v_mov_b32_e32 v55, v50
	v_pk_add_f32 v[42:43], v[54:55], v[42:43]
	v_mov_b32_e32 v50, v57
	v_pk_add_f32 v[42:43], v[50:51], v[42:43]
	v_lshlrev_b32_e32 v56, 16, v18
	v_and_b32_e32 v57, 0xffff0000, v18
	v_mul_f32_e32 v18, 0xbfb8aa3b, v56
	v_exp_f32_e32 v18, v18
	v_add_f32_dpp v42, v42, v42 quad_perm:[1,0,3,2] row_mask:0xf bank_mask:0xf
	v_add_f32_dpp v43, v43, v43 quad_perm:[1,0,3,2] row_mask:0xf bank_mask:0xf
	v_mul_f32_e32 v58, 0xbfb8aa3b, v57
	v_exp_f32_e32 v59, v58
	v_add_f32_e32 v18, 1.0, v18
	s_mov_b32 s0, 0x3c800000
	v_add_f32_dpp v42, v42, v42 quad_perm:[2,3,0,1] row_mask:0xf bank_mask:0xf
	v_add_f32_dpp v43, v43, v43 quad_perm:[2,3,0,1] row_mask:0xf bank_mask:0xf
	v_rcp_f32_e32 v58, v18
	v_add_f32_e32 v18, 1.0, v59
	v_rcp_f32_e32 v59, v18
	v_and_b32_e32 v31, 0xffff0000, v31
	v_add_f32_dpp v42, v42, v42 row_half_mirror row_mask:0xf bank_mask:0xf
	v_add_f32_dpp v43, v43, v43 row_half_mirror row_mask:0xf bank_mask:0xf
	v_mul_f32_e32 v55, 0xbfb8aa3b, v31
	v_exp_f32_e32 v55, v55
	v_add_f32_e32 v54, 1.0, v60
	v_rcp_f32_e32 v54, v54
	v_add_f32_dpp v42, v42, v42 row_mirror row_mask:0xf bank_mask:0xf
	v_add_f32_dpp v43, v43, v43 row_mirror row_mask:0xf bank_mask:0xf
	v_add_f32_e32 v55, 1.0, v55
	v_pk_fma_f32 v[42:43], v[42:43], s[0:1], v[196:197] op_sel_hi:[1,0,0]
	v_rcp_f32_e32 v55, v55
	v_mul_f32_e32 v18, 0x4b800000, v43
	v_cmp_gt_f32_e32 vcc, s63, v43
	v_lshl_add_u64 v[50:51], s[28:29], 0, v[2:3]
	v_pk_mul_f32 v[30:31], v[54:55], v[30:31]
	v_cndmask_b32_e32 v18, v43, v18, vcc
	v_rsq_f32_e32 v18, v18
	s_mov_b32 s0, 0xb80000
	s_add_i32 s24, s24, 1
	v_pk_mul_f32 v[54:55], v[58:59], v[56:57]
	v_mul_f32_e32 v43, 0x45800000, v18
	v_cndmask_b32_e32 v18, v18, v43, vcc
	v_pk_mul_f32 v[32:33], v[32:33], v[18:19] op_sel_hi:[1,0]
	v_cmp_gt_f32_e32 vcc, s63, v42
	v_pk_mul_f32 v[32:33], v[4:5], v[32:33]
	s_add_u32 s20, s20, 0x1a80
	v_pk_mul_f32 v[32:33], v[40:41], v[32:33]
	v_pk_mul_f32 v[40:41], v[48:49], v[18:19] op_sel_hi:[1,0]
	v_mul_f32_e32 v18, 0x4b800000, v42
	v_cndmask_b32_e32 v18, v42, v18, vcc
	v_pk_mul_f32 v[40:41], v[6:7], v[40:41]
	v_rsq_f32_e32 v18, v18
	v_pk_mul_f32 v[30:31], v[30:31], v[40:41]
	v_cvt_pk_bf16_f32 v32, v32, v33
	v_cvt_pk_bf16_f32 v33, v30, v31
	v_add_co_u32_e64 v30, s[0:1], s0, v50
	s_addc_u32 s21, s21, 0
	s_nop 0
	v_addc_co_u32_e64 v31, s[0:1], 0, v51, s[0:1]
	global_store_dwordx2 v[30:31], v[32:33], off offset:2560 sc1
	v_mul_f32_e32 v30, 0x45800000, v18
	v_cndmask_b32_e32 v18, v18, v30, vcc
	v_lshlrev_b32_e32 v30, 16, v19
	v_and_b32_e32 v31, 0xffff0000, v19
	v_mul_f32_e32 v19, 0xbfb8aa3b, v30
	v_exp_f32_e32 v19, v19
	v_mul_f32_e32 v32, 0xbfb8aa3b, v31
	v_exp_f32_e32 v40, v32
	s_mov_b32 s0, 0xb81000
	v_pk_mul_f32 v[32:33], v[38:39], v[18:19] op_sel_hi:[1,0]
	v_add_f32_e32 v19, 1.0, v19
	v_rcp_f32_e32 v38, v19
	v_add_f32_e32 v19, 1.0, v40
	v_rcp_f32_e32 v39, v19
	v_pk_mul_f32 v[18:19], v[52:53], v[18:19] op_sel_hi:[1,0]
	v_pk_mul_f32 v[32:33], v[54:55], v[32:33]
	s_add_u32 s28, s28, 0x1a80
	v_pk_mul_f32 v[30:31], v[38:39], v[30:31]
	v_cvt_pk_bf16_f32 v32, v32, v33
	v_pk_mul_f32 v[18:19], v[30:31], v[18:19]
	s_addc_u32 s29, s29, 0
	v_cvt_pk_bf16_f32 v33, v18, v19
	v_add_co_u32_e32 v18, vcc, s0, v50
	s_cmp_ge_i32 s24, s2
	s_nop 0
	v_addc_co_u32_e32 v19, vcc, 0, v51, vcc
	global_store_dwordx2 v[18:19], v[32:33], off offset:512 sc1
	v_mov_b64_e32 v[18:19], v[20:21]
	v_mov_b64_e32 v[30:31], v[16:17]
	v_mov_b64_e32 v[32:33], v[10:11]
	v_mov_b64_e32 v[42:43], v[12:13]
	v_mov_b64_e32 v[38:39], v[14:15]
	v_mov_b64_e32 v[40:41], v[8:9]
	s_waitcnt vmcnt(2)
	v_mov_b64_e32 v[20:21], v[36:37]
	v_mov_b64_e32 v[16:17], v[34:35]
	v_mov_b64_e32 v[10:11], v[22:23]
	v_mov_b64_e32 v[12:13], v[24:25]
	v_mov_b64_e32 v[14:15], v[26:27]
	v_mov_b64_e32 v[8:9], v[28:29]
	s_cbranch_scc1 .LBB0_248
